# bundle25 + attention: second half of next-unit prefetch/address block interleaved between the QK MFMAs
# baseline (speedup 1.0000x reference)
.LBB0_412:
	s_and_b32 s49, s38, 1
	s_mul_i32 s101, s49, 0x12000
	v_add3_u32 v56, s101, v182, v215
	v_add3_u32 v64, s101, v183, v215
	ds_read_b128 v[52:55], v56
	ds_read_b128 v[56:59], v56 offset:64
	ds_read_b128 v[60:63], v64
	ds_read_b128 v[66:69], v64 offset:64
	v_add3_u32 v64, s101, v184, v215
	ds_read_b128 v[70:73], v64
	ds_read_b128 v[74:77], v64 offset:64
	v_add3_u32 v64, s101, v185, v215
	ds_read_b128 v[90:93], v64
	ds_read_b128 v[94:97], v64 offset:64
	v_add3_u32 v64, s101, v186, v215
	ds_read_b128 v[98:101], v64
	ds_read_b128 v[102:105], v64 offset:64
	v_add3_u32 v64, s101, v187, v215
	ds_read_b128 v[106:109], v64
	ds_read_b128 v[110:113], v64 offset:64
	v_add3_u32 v64, s101, v188, v215
	ds_read_b128 v[114:117], v64
	ds_read_b128 v[118:121], v64 offset:64
	v_add3_u32 v64, s101, v189, v215
	ds_read_b128 v[122:125], v64
	ds_read_b128 v[126:129], v64 offset:64
	v_add3_u32 v64, s101, v190, v215
	ds_read_b128 v[130:133], v64
	ds_read_b128 v[134:137], v64 offset:64
	s_mul_hi_i32 s23, s39, 0x2aaaaaab
	s_lshr_b32 s24, s23, 31
	s_ashr_i32 s23, s23, 5
	s_add_i32 s34, s23, s24
	s_mul_i32 s23, s34, 0xffffff40
	s_add_i32 s23, s39, s23
	s_mov_b32 s31, s25
	s_and_b32 s49, s38, 1
	s_xor_b32 s100, s49, 1
	s_mul_i32 s100, s100, 0x12000
	s_ashr_i32 s24, s23, 6
	s_and_b32 s25, s39, 63
	s_ashr_i32 s36, s34, 4
	s_cmp_eq_u32 s24, 1
	s_cselect_b64 s[26:27], -1, 0
	s_and_b64 s[28:29], s[26:27], exec
	s_cselect_b32 s35, 3, 15
	s_cselect_b32 s37, 2, 4
	s_cmp_lt_u32 s23, 64
	s_cselect_b64 s[28:29], -1, 0
	s_and_b64 s[56:57], s[28:29], exec
	s_cselect_b32 s62, 0, s37
	s_waitcnt vmcnt(2)
	v_mov_b64_e32 v[88:89], v[10:11]
	s_cselect_b32 s23, 0, s35
	s_lshr_b32 s25, s25, s62
	s_waitcnt vmcnt(1)
	v_mov_b64_e32 v[50:51], v[14:15]
	v_mov_b64_e32 v[86:87], v[8:9]
	v_sub_u32_e64 v8, s25, 1 clamp
	v_mov_b64_e32 v[48:49], v[12:13]
	s_ashr_i32 s35, s34, 31
	v_lshlrev_b32_e32 v12, 7, v8
	s_and_b32 s23, s23, s70
	s_lshl_b64 s[56:57], s[34:35], 13
	s_or_b32 s56, s56, s23
	s_waitcnt lgkmcnt(14)
	v_mfma_f32_16x16x32_bf16 v[52:55], v[52:55], v[86:89], v[4:7]
	v_mov_b32_e32 v204, s56
	v_or_b32_e32 v8, v12, v172
	v_lshl_add_u32 v8, v8, s62, v204
	v_mfma_f32_16x16x32_bf16 v[82:85], v[56:59], v[48:51], v[52:55]
	v_lshl_or_b32 v8, v8, 7, v191
	global_load_dwordx4 v[16:19], v8, s[76:77]
	global_load_dwordx4 v[20:23], v8, s[78:79]
	v_mfma_f32_16x16x32_bf16 v[52:55], v[60:63], v[86:89], 0
	v_or_b32_e32 v8, v12, v174
	v_lshl_add_u32 v8, v8, s62, v204
	v_lshl_or_b32 v8, v8, 7, v191
	v_mfma_f32_16x16x32_bf16 v[78:81], v[66:69], v[48:51], v[52:55]
	s_lshl_b32 s63, s25, 7
	global_load_dwordx4 v[24:27], v8, s[76:77]
	global_load_dwordx4 v[28:31], v8, s[78:79]
	s_waitcnt lgkmcnt(13)
	v_mfma_f32_16x16x32_bf16 v[52:55], v[70:73], v[86:89], 0
	v_or_b32_e32 v8, s63, v172
	v_lshl_add_u32 v8, v8, s62, v204
	v_lshl_or_b32 v8, v8, 7, v191
	s_waitcnt lgkmcnt(12)
	v_mfma_f32_16x16x32_bf16 v[74:77], v[74:77], v[48:51], v[52:55]
	global_load_dwordx4 v[32:35], v8, s[76:77]
	global_load_dwordx4 v[36:39], v8, s[78:79]
	v_or_b32_e32 v8, s63, v175
	s_waitcnt lgkmcnt(11)
	v_mfma_f32_16x16x32_bf16 v[52:55], v[90:93], v[86:89], 0
	v_lshl_add_u32 v8, v8, s62, v204
	v_lshl_or_b32 v8, v8, 7, v191
	global_load_dwordx4 v[40:43], v8, s[76:77]
	s_waitcnt lgkmcnt(10)
	v_mfma_f32_16x16x32_bf16 v[70:73], v[94:97], v[48:51], v[52:55]
	global_load_dwordx4 v[44:47], v8, s[78:79]
	s_ashr_i32 s37, s36, 31
	v_add_u32_e32 v8, s63, v181
	s_waitcnt lgkmcnt(9)
	v_mfma_f32_16x16x32_bf16 v[52:55], v[98:101], v[86:89], 0
	s_lshl_b64 s[36:37], s[36:37], 13
	v_ashrrev_i32_e32 v9, 31, v8
	s_or_b32 s36, s36, s23
	s_waitcnt lgkmcnt(8)
	v_mfma_f32_16x16x32_bf16 v[66:69], v[102:105], v[48:51], v[52:55]
	v_lshlrev_b64 v[8:9], s62, v[8:9]
	v_lshl_add_u64 v[164:165], s[36:37], 0, v[8:9]
	v_lshlrev_b64 v[162:163], 6, v[164:165]
	s_waitcnt lgkmcnt(7)
	v_mfma_f32_16x16x32_bf16 v[52:55], v[106:109], v[86:89], 0
	s_lshl_b64 s[36:37], s[34:35], 20
	s_add_u32 s36, s64, s36
	v_lshlrev_b32_e32 v8, 1, v162
	s_waitcnt lgkmcnt(6)
	v_mfma_f32_16x16x32_bf16 v[60:63], v[110:113], v[48:51], v[52:55]
	s_addc_u32 s37, s65, s37
	v_and_b32_e32 v64, 0xfff80, v8
	v_lshl_add_u64 v[8:9], s[36:37], 0, v[64:65]
	s_waitcnt lgkmcnt(5)
	v_mfma_f32_16x16x32_bf16 v[52:55], v[114:117], v[86:89], 0
	v_mov_b32_e32 v169, v65
	v_lshl_add_u64 v[12:13], v[8:9], 0, v[168:169]
	global_load_dwordx4 v[8:11], v[12:13], off
	s_waitcnt lgkmcnt(4)
	v_mfma_f32_16x16x32_bf16 v[56:59], v[118:121], v[48:51], v[52:55]
	s_nop 0
	global_load_dwordx4 v[12:15], v[12:13], off offset:64
	s_waitcnt lgkmcnt(3)
	v_mfma_f32_16x16x32_bf16 v[52:55], v[122:125], v[86:89], 0
	s_waitcnt lgkmcnt(1)
	v_mfma_f32_16x16x32_bf16 v[86:89], v[130:133], v[86:89], v[0:3]
	v_mfma_f32_16x16x32_bf16 v[52:55], v[126:129], v[48:51], v[52:55]
	s_waitcnt lgkmcnt(0)
	v_mfma_f32_16x16x32_bf16 v[48:51], v[134:137], v[48:51], v[86:89]
	s_cmp_lg_u32 s31, 0
	s_cbranch_scc1 .LBB0_414
	s_nop 3
	v_pk_add_f32 v[86:87], v[84:85], s[84:85] op_sel_hi:[1,0]
	v_pk_add_f32 v[88:89], v[82:83], s[84:85] op_sel_hi:[1,0]
	v_cndmask_b32_e64 v85, v85, v87, s[20:21]
	v_cndmask_b32_e64 v84, v84, v86, s[20:21]
	v_cndmask_b32_e64 v83, v83, v89, s[20:21]
	v_cndmask_b32_e64 v82, v82, v88, s[20:21]
	v_pk_add_f32 v[86:87], v[80:81], s[84:85] op_sel_hi:[1,0]
	v_pk_add_f32 v[88:89], v[78:79], s[84:85] op_sel_hi:[1,0]
	v_cndmask_b32_e64 v81, v81, v87, s[18:19]
	v_cndmask_b32_e64 v80, v80, v86, s[18:19]
	v_cndmask_b32_e64 v79, v79, v89, s[18:19]
	v_cndmask_b32_e64 v78, v78, v88, s[18:19]
	v_pk_add_f32 v[86:87], v[76:77], s[84:85] op_sel_hi:[1,0]
	v_pk_add_f32 v[88:89], v[74:75], s[84:85] op_sel_hi:[1,0]
	v_cndmask_b32_e64 v77, v77, v87, s[16:17]
	v_cndmask_b32_e64 v76, v76, v86, s[16:17]
	v_cndmask_b32_e64 v75, v75, v89, s[16:17]
	v_cndmask_b32_e64 v74, v74, v88, s[16:17]
	v_pk_add_f32 v[86:87], v[72:73], s[84:85] op_sel_hi:[1,0]
	v_pk_add_f32 v[88:89], v[70:71], s[84:85] op_sel_hi:[1,0]
	v_cndmask_b32_e64 v73, v73, v87, s[14:15]
	v_cndmask_b32_e64 v72, v72, v86, s[14:15]
	v_cndmask_b32_e64 v71, v71, v89, s[14:15]
	v_cndmask_b32_e64 v70, v70, v88, s[14:15]
	v_pk_add_f32 v[86:87], v[68:69], s[84:85] op_sel_hi:[1,0]
	v_pk_add_f32 v[88:89], v[66:67], s[84:85] op_sel_hi:[1,0]
	v_cndmask_b32_e64 v69, v69, v87, s[12:13]
	v_cndmask_b32_e64 v68, v68, v86, s[12:13]
	v_cndmask_b32_e64 v67, v67, v89, s[12:13]
	v_cndmask_b32_e64 v66, v66, v88, s[12:13]
	v_pk_add_f32 v[86:87], v[62:63], s[84:85] op_sel_hi:[1,0]
	v_pk_add_f32 v[88:89], v[60:61], s[84:85] op_sel_hi:[1,0]
	v_cndmask_b32_e64 v63, v63, v87, s[10:11]
	v_cndmask_b32_e64 v62, v62, v86, s[10:11]
	v_cndmask_b32_e64 v61, v61, v89, s[10:11]
	v_cndmask_b32_e64 v60, v60, v88, s[10:11]
	v_pk_add_f32 v[86:87], v[58:59], s[84:85] op_sel_hi:[1,0]
	v_pk_add_f32 v[88:89], v[56:57], s[84:85] op_sel_hi:[1,0]
	v_cndmask_b32_e64 v59, v59, v87, s[8:9]
	v_cndmask_b32_e64 v58, v58, v86, s[8:9]
	v_cndmask_b32_e64 v57, v57, v89, s[8:9]
	v_cndmask_b32_e64 v56, v56, v88, s[8:9]
	v_pk_add_f32 v[86:87], v[54:55], s[84:85] op_sel_hi:[1,0]
	v_pk_add_f32 v[88:89], v[52:53], s[84:85] op_sel_hi:[1,0]
	v_cndmask_b32_e64 v55, v55, v87, s[6:7]
	v_cndmask_b32_e64 v54, v54, v86, s[6:7]
	v_cndmask_b32_e64 v53, v53, v89, s[6:7]
	v_cndmask_b32_e64 v52, v52, v88, s[6:7]
